# 32-wide k-snake (each A fragment's four MFMA pairs consecutive, pairs back to back with alternating k) in 4 GEMM loops, same stack as v100
# baseline (speedup 1.0000x reference)
.LBB0_114:
	ds_read_b128 v[130:133], v220
	ds_read_b128 v[134:137], v220 offset:1024
	ds_read_b128 v[138:141], v220 offset:2048
	ds_read_b128 v[142:145], v220 offset:3072
	ds_read_b128 v[146:149], v221
	ds_read_b128 v[150:153], v221 offset:1024
	ds_read_b128 v[154:157], v221 offset:2048
	ds_read_b128 v[158:161], v221 offset:3072
	s_add_i32 s46, s64, 0xfff80080
	s_cmp_eq_u32 s84, 28
	s_cselect_b32 s87, s62, s46
	s_cselect_b32 s86, s63, s65
	s_or_b32 s85, s87, 0x80
	s_mov_b32 m0, s93
	ds_read_b128 v[162:165], v222
	ds_read_b128 v[166:169], v222 offset:1024
	ds_read_b128 v[170:173], v222 offset:2048
	ds_read_b128 v[174:177], v222 offset:3072
	ds_read_b128 v[178:181], v222 offset:4096
	ds_read_b128 v[182:185], v222 offset:5120
	ds_read_b128 v[186:189], v222 offset:6144
	ds_read_b128 v[212:215], v222 offset:7168
	buffer_load_dwordx4 v1, s[40:43], s64 offen lds
	s_mov_b32 m0, s94
	s_nop 0
	buffer_load_dwordx4 v216, s[40:43], s64 offen lds
	s_waitcnt vmcnt(8)
	s_waitcnt lgkmcnt(0)
	s_barrier
	s_waitcnt lgkmcnt(7)
	v_mfma_f32_16x16x32_bf16 v[126:129], v[130:133], v[162:165], v[126:129]
	v_mfma_f32_16x16x32_bf16 v[126:129], v[134:137], v[166:169], v[126:129]
	s_waitcnt lgkmcnt(5)
	v_mfma_f32_16x16x32_bf16 v[122:125], v[142:145], v[166:169], v[122:125]
	v_mfma_f32_16x16x32_bf16 v[122:125], v[138:141], v[162:165], v[122:125]
	s_waitcnt lgkmcnt(3)
	v_mfma_f32_16x16x32_bf16 v[118:121], v[146:149], v[162:165], v[118:121]
	v_mfma_f32_16x16x32_bf16 v[118:121], v[150:153], v[166:169], v[118:121]
	s_waitcnt lgkmcnt(1)
	v_mfma_f32_16x16x32_bf16 v[110:113], v[158:161], v[166:169], v[110:113]
	v_mfma_f32_16x16x32_bf16 v[110:113], v[154:157], v[162:165], v[110:113]
	v_mfma_f32_16x16x32_bf16 v[90:93], v[154:157], v[170:173], v[90:93]
	v_mfma_f32_16x16x32_bf16 v[90:93], v[158:161], v[174:177], v[90:93]
	v_mfma_f32_16x16x32_bf16 v[98:101], v[150:153], v[174:177], v[98:101]
	v_mfma_f32_16x16x32_bf16 v[98:101], v[146:149], v[170:173], v[98:101]
	v_mfma_f32_16x16x32_bf16 v[106:109], v[138:141], v[170:173], v[106:109]
	v_mfma_f32_16x16x32_bf16 v[106:109], v[142:145], v[174:177], v[106:109]
	s_waitcnt lgkmcnt(0)
	v_mfma_f32_16x16x32_bf16 v[114:117], v[134:137], v[174:177], v[114:117]
	v_mfma_f32_16x16x32_bf16 v[114:117], v[130:133], v[170:173], v[114:117]
	v_mfma_f32_16x16x32_bf16 v[102:105], v[130:133], v[178:181], v[102:105]
	v_mfma_f32_16x16x32_bf16 v[102:105], v[134:137], v[182:185], v[102:105]
	v_mfma_f32_16x16x32_bf16 v[94:97], v[142:145], v[182:185], v[94:97]
	v_mfma_f32_16x16x32_bf16 v[94:97], v[138:141], v[178:181], v[94:97]
	v_mfma_f32_16x16x32_bf16 v[82:85], v[146:149], v[178:181], v[82:85]
	v_mfma_f32_16x16x32_bf16 v[82:85], v[150:153], v[182:185], v[82:85]
	v_mfma_f32_16x16x32_bf16 v[74:77], v[158:161], v[182:185], v[74:77]
	v_mfma_f32_16x16x32_bf16 v[74:77], v[154:157], v[178:181], v[74:77]
	v_mfma_f32_16x16x32_bf16 v[66:69], v[154:157], v[186:189], v[66:69]
	v_mfma_f32_16x16x32_bf16 v[66:69], v[158:161], v[212:215], v[66:69]
	v_mfma_f32_16x16x32_bf16 v[70:73], v[150:153], v[212:215], v[70:73]
	v_mfma_f32_16x16x32_bf16 v[70:73], v[146:149], v[186:189], v[70:73]
	v_mfma_f32_16x16x32_bf16 v[78:81], v[138:141], v[186:189], v[78:81]
	v_mfma_f32_16x16x32_bf16 v[78:81], v[142:145], v[212:215], v[78:81]
	v_mfma_f32_16x16x32_bf16 v[86:89], v[134:137], v[212:215], v[86:89]
	v_mfma_f32_16x16x32_bf16 v[86:89], v[130:133], v[186:189], v[86:89]
	s_barrier
	s_mov_b32 m0, s69
	s_mov_b32 s46, s42
	s_mov_b32 s47, s43
	ds_read_b128 v[162:165], v222 offset:16384
	ds_read_b128 v[166:169], v222 offset:17408
	ds_read_b128 v[170:173], v222 offset:18432
	ds_read_b128 v[174:177], v222 offset:19456
	ds_read_b128 v[178:181], v222 offset:20480
	ds_read_b128 v[182:185], v222 offset:21504
	ds_read_b128 v[186:189], v222 offset:22528
	ds_read_b128 v[212:215], v222 offset:23552
	buffer_load_dwordx4 v191, s[44:47], s86 offen lds
	s_mov_b32 m0, s70
	s_add_i32 s88, s86, 0x80000
	buffer_load_dwordx4 v217, s[44:47], s86 offen lds
	s_mov_b32 m0, s71
	s_nop 0
	buffer_load_dwordx4 v191, s[44:47], s88 offen lds
	s_mov_b32 m0, s72
	s_nop 0
	buffer_load_dwordx4 v217, s[44:47], s88 offen lds
	s_mov_b32 m0, s68
	s_nop 0
	buffer_load_dwordx4 v1, s[40:43], s87 offen lds
	s_mov_b32 m0, s73
	s_nop 0
	buffer_load_dwordx4 v216, s[40:43], s87 offen lds
	s_waitcnt vmcnt(8)
	s_waitcnt lgkmcnt(0)
	s_barrier
	s_waitcnt lgkmcnt(7)
	v_mfma_f32_16x16x32_bf16 v[62:65], v[130:133], v[162:165], v[62:65]
	v_mfma_f32_16x16x32_bf16 v[62:65], v[134:137], v[166:169], v[62:65]
	s_waitcnt lgkmcnt(5)
	v_mfma_f32_16x16x32_bf16 v[58:61], v[142:145], v[166:169], v[58:61]
	v_mfma_f32_16x16x32_bf16 v[58:61], v[138:141], v[162:165], v[58:61]
	s_waitcnt lgkmcnt(3)
	v_mfma_f32_16x16x32_bf16 v[50:53], v[146:149], v[162:165], v[50:53]
	v_mfma_f32_16x16x32_bf16 v[50:53], v[150:153], v[166:169], v[50:53]
	s_waitcnt lgkmcnt(1)
	v_mfma_f32_16x16x32_bf16 v[42:45], v[158:161], v[166:169], v[42:45]
	v_mfma_f32_16x16x32_bf16 v[42:45], v[154:157], v[162:165], v[42:45]
	v_mfma_f32_16x16x32_bf16 v[26:29], v[154:157], v[170:173], v[26:29]
	v_mfma_f32_16x16x32_bf16 v[26:29], v[158:161], v[174:177], v[26:29]
	v_mfma_f32_16x16x32_bf16 v[34:37], v[150:153], v[174:177], v[34:37]
	v_mfma_f32_16x16x32_bf16 v[34:37], v[146:149], v[170:173], v[34:37]
	v_mfma_f32_16x16x32_bf16 v[46:49], v[138:141], v[170:173], v[46:49]
	v_mfma_f32_16x16x32_bf16 v[46:49], v[142:145], v[174:177], v[46:49]
	s_waitcnt lgkmcnt(0)
	v_mfma_f32_16x16x32_bf16 v[54:57], v[134:137], v[174:177], v[54:57]
	v_mfma_f32_16x16x32_bf16 v[54:57], v[130:133], v[170:173], v[54:57]
	v_mfma_f32_16x16x32_bf16 v[38:41], v[130:133], v[178:181], v[38:41]
	v_mfma_f32_16x16x32_bf16 v[38:41], v[134:137], v[182:185], v[38:41]
	v_mfma_f32_16x16x32_bf16 v[30:33], v[142:145], v[182:185], v[30:33]
	v_mfma_f32_16x16x32_bf16 v[30:33], v[138:141], v[178:181], v[30:33]
	v_mfma_f32_16x16x32_bf16 v[18:21], v[146:149], v[178:181], v[18:21]
	v_mfma_f32_16x16x32_bf16 v[18:21], v[150:153], v[182:185], v[18:21]
	v_mfma_f32_16x16x32_bf16 v[10:13], v[158:161], v[182:185], v[10:13]
	v_mfma_f32_16x16x32_bf16 v[10:13], v[154:157], v[178:181], v[10:13]
	v_mfma_f32_16x16x32_bf16 v[2:5], v[154:157], v[186:189], v[2:5]
	v_mfma_f32_16x16x32_bf16 v[2:5], v[158:161], v[212:215], v[2:5]
	v_mfma_f32_16x16x32_bf16 v[6:9], v[150:153], v[212:215], v[6:9]
	v_mfma_f32_16x16x32_bf16 v[6:9], v[146:149], v[186:189], v[6:9]
	v_mfma_f32_16x16x32_bf16 v[14:17], v[138:141], v[186:189], v[14:17]
	v_mfma_f32_16x16x32_bf16 v[14:17], v[142:145], v[212:215], v[14:17]
	v_mfma_f32_16x16x32_bf16 v[22:25], v[134:137], v[212:215], v[22:25]
	v_mfma_f32_16x16x32_bf16 v[22:25], v[130:133], v[186:189], v[22:25]
	s_barrier
	ds_read_b128 v[130:133], v223
	ds_read_b128 v[134:137], v223 offset:1024
	ds_read_b128 v[138:141], v223 offset:2048
	ds_read_b128 v[142:145], v223 offset:3072
	ds_read_b128 v[146:149], v224
	ds_read_b128 v[150:153], v224 offset:1024
	ds_read_b128 v[154:157], v224 offset:2048
	ds_read_b128 v[158:161], v224 offset:3072
	s_add_i32 s87, s87, 0x80000
	s_mov_b32 m0, s74
	ds_read_b128 v[162:165], v222 offset:32768
	ds_read_b128 v[166:169], v222 offset:33792
	ds_read_b128 v[170:173], v222 offset:34816
	ds_read_b128 v[174:177], v222 offset:35840
	ds_read_b128 v[178:181], v222 offset:36864
	ds_read_b128 v[182:185], v222 offset:37888
	ds_read_b128 v[186:189], v222 offset:38912
	ds_read_b128 v[212:215], v222 offset:39936
	buffer_load_dwordx4 v1, s[40:43], s87 offen lds
	s_mov_b32 m0, s75
	s_nop 0
	buffer_load_dwordx4 v216, s[40:43], s87 offen lds
	s_waitcnt vmcnt(8)
	s_waitcnt lgkmcnt(0)
	s_barrier
	s_waitcnt lgkmcnt(7)
	v_mfma_f32_16x16x32_bf16 v[126:129], v[130:133], v[162:165], v[126:129]
	v_mfma_f32_16x16x32_bf16 v[126:129], v[134:137], v[166:169], v[126:129]
	s_waitcnt lgkmcnt(5)
	v_mfma_f32_16x16x32_bf16 v[122:125], v[142:145], v[166:169], v[122:125]
	v_mfma_f32_16x16x32_bf16 v[122:125], v[138:141], v[162:165], v[122:125]
	s_waitcnt lgkmcnt(3)
	v_mfma_f32_16x16x32_bf16 v[118:121], v[146:149], v[162:165], v[118:121]
	v_mfma_f32_16x16x32_bf16 v[118:121], v[150:153], v[166:169], v[118:121]
	s_waitcnt lgkmcnt(1)
	v_mfma_f32_16x16x32_bf16 v[110:113], v[158:161], v[166:169], v[110:113]
	v_mfma_f32_16x16x32_bf16 v[110:113], v[154:157], v[162:165], v[110:113]
	v_mfma_f32_16x16x32_bf16 v[90:93], v[154:157], v[170:173], v[90:93]
	v_mfma_f32_16x16x32_bf16 v[90:93], v[158:161], v[174:177], v[90:93]
	v_mfma_f32_16x16x32_bf16 v[98:101], v[150:153], v[174:177], v[98:101]
	v_mfma_f32_16x16x32_bf16 v[98:101], v[146:149], v[170:173], v[98:101]
	v_mfma_f32_16x16x32_bf16 v[106:109], v[138:141], v[170:173], v[106:109]
	v_mfma_f32_16x16x32_bf16 v[106:109], v[142:145], v[174:177], v[106:109]
	s_waitcnt lgkmcnt(0)
	v_mfma_f32_16x16x32_bf16 v[114:117], v[134:137], v[174:177], v[114:117]
	v_mfma_f32_16x16x32_bf16 v[114:117], v[130:133], v[170:173], v[114:117]
	v_mfma_f32_16x16x32_bf16 v[102:105], v[130:133], v[178:181], v[102:105]
	v_mfma_f32_16x16x32_bf16 v[102:105], v[134:137], v[182:185], v[102:105]
	v_mfma_f32_16x16x32_bf16 v[94:97], v[142:145], v[182:185], v[94:97]
	v_mfma_f32_16x16x32_bf16 v[94:97], v[138:141], v[178:181], v[94:97]
	v_mfma_f32_16x16x32_bf16 v[82:85], v[146:149], v[178:181], v[82:85]
	v_mfma_f32_16x16x32_bf16 v[82:85], v[150:153], v[182:185], v[82:85]
	v_mfma_f32_16x16x32_bf16 v[74:77], v[158:161], v[182:185], v[74:77]
	v_mfma_f32_16x16x32_bf16 v[74:77], v[154:157], v[178:181], v[74:77]
	v_mfma_f32_16x16x32_bf16 v[66:69], v[154:157], v[186:189], v[66:69]
	v_mfma_f32_16x16x32_bf16 v[66:69], v[158:161], v[212:215], v[66:69]
	v_mfma_f32_16x16x32_bf16 v[70:73], v[150:153], v[212:215], v[70:73]
	v_mfma_f32_16x16x32_bf16 v[70:73], v[146:149], v[186:189], v[70:73]
	v_mfma_f32_16x16x32_bf16 v[78:81], v[138:141], v[186:189], v[78:81]
	v_mfma_f32_16x16x32_bf16 v[78:81], v[142:145], v[212:215], v[78:81]
	v_mfma_f32_16x16x32_bf16 v[86:89], v[134:137], v[212:215], v[86:89]
	v_mfma_f32_16x16x32_bf16 v[86:89], v[130:133], v[186:189], v[86:89]
	s_barrier
	s_mov_b32 m0, s79
	s_or_b32 s87, s86, 0x80
	ds_read_b128 v[162:165], v222 offset:49152
	ds_read_b128 v[166:169], v222 offset:50176
	ds_read_b128 v[170:173], v222 offset:51200
	ds_read_b128 v[174:177], v222 offset:52224
	ds_read_b128 v[178:181], v222 offset:53248
	ds_read_b128 v[182:185], v222 offset:54272
	ds_read_b128 v[186:189], v222 offset:55296
	ds_read_b128 v[212:215], v222 offset:56320
	buffer_load_dwordx4 v191, s[44:47], s87 offen lds
	s_mov_b32 m0, s80
	s_add_i32 s86, s86, 0x80080
	buffer_load_dwordx4 v217, s[44:47], s87 offen lds
	s_mov_b32 m0, s83
	s_nop 0
	buffer_load_dwordx4 v191, s[44:47], s86 offen lds
	s_mov_b32 m0, s92
	s_nop 0
	buffer_load_dwordx4 v217, s[44:47], s86 offen lds
	s_mov_b32 m0, s81
	s_nop 0
	buffer_load_dwordx4 v1, s[40:43], s85 offen lds
	s_mov_b32 m0, s82
	s_nop 0
	buffer_load_dwordx4 v216, s[40:43], s85 offen lds
	s_waitcnt vmcnt(8)
	s_waitcnt lgkmcnt(0)
	s_barrier
	s_waitcnt lgkmcnt(7)
	v_mfma_f32_16x16x32_bf16 v[62:65], v[130:133], v[162:165], v[62:65]
	v_mfma_f32_16x16x32_bf16 v[62:65], v[134:137], v[166:169], v[62:65]
	s_waitcnt lgkmcnt(5)
	v_mfma_f32_16x16x32_bf16 v[58:61], v[142:145], v[166:169], v[58:61]
	v_mfma_f32_16x16x32_bf16 v[58:61], v[138:141], v[162:165], v[58:61]
	s_waitcnt lgkmcnt(3)
	v_mfma_f32_16x16x32_bf16 v[50:53], v[146:149], v[162:165], v[50:53]
	v_mfma_f32_16x16x32_bf16 v[50:53], v[150:153], v[166:169], v[50:53]
	s_waitcnt lgkmcnt(1)
	v_mfma_f32_16x16x32_bf16 v[42:45], v[158:161], v[166:169], v[42:45]
	v_mfma_f32_16x16x32_bf16 v[42:45], v[154:157], v[162:165], v[42:45]
	v_mfma_f32_16x16x32_bf16 v[26:29], v[154:157], v[170:173], v[26:29]
	v_mfma_f32_16x16x32_bf16 v[26:29], v[158:161], v[174:177], v[26:29]
	v_mfma_f32_16x16x32_bf16 v[34:37], v[150:153], v[174:177], v[34:37]
	v_mfma_f32_16x16x32_bf16 v[34:37], v[146:149], v[170:173], v[34:37]
	v_mfma_f32_16x16x32_bf16 v[46:49], v[138:141], v[170:173], v[46:49]
	v_mfma_f32_16x16x32_bf16 v[46:49], v[142:145], v[174:177], v[46:49]
	s_waitcnt lgkmcnt(0)
	v_mfma_f32_16x16x32_bf16 v[54:57], v[134:137], v[174:177], v[54:57]
	v_mfma_f32_16x16x32_bf16 v[54:57], v[130:133], v[170:173], v[54:57]
	v_mfma_f32_16x16x32_bf16 v[38:41], v[130:133], v[178:181], v[38:41]
	v_mfma_f32_16x16x32_bf16 v[38:41], v[134:137], v[182:185], v[38:41]
	v_mfma_f32_16x16x32_bf16 v[30:33], v[142:145], v[182:185], v[30:33]
	v_mfma_f32_16x16x32_bf16 v[30:33], v[138:141], v[178:181], v[30:33]
	v_mfma_f32_16x16x32_bf16 v[18:21], v[146:149], v[178:181], v[18:21]
	v_mfma_f32_16x16x32_bf16 v[18:21], v[150:153], v[182:185], v[18:21]
	v_mfma_f32_16x16x32_bf16 v[10:13], v[158:161], v[182:185], v[10:13]
	v_mfma_f32_16x16x32_bf16 v[10:13], v[154:157], v[178:181], v[10:13]
	v_mfma_f32_16x16x32_bf16 v[2:5], v[154:157], v[186:189], v[2:5]
	v_mfma_f32_16x16x32_bf16 v[2:5], v[158:161], v[212:215], v[2:5]
	v_mfma_f32_16x16x32_bf16 v[6:9], v[150:153], v[212:215], v[6:9]
	v_mfma_f32_16x16x32_bf16 v[6:9], v[146:149], v[186:189], v[6:9]
	v_mfma_f32_16x16x32_bf16 v[14:17], v[138:141], v[186:189], v[14:17]
	v_mfma_f32_16x16x32_bf16 v[14:17], v[142:145], v[212:215], v[14:17]
	v_mfma_f32_16x16x32_bf16 v[22:25], v[134:137], v[212:215], v[22:25]
	v_mfma_f32_16x16x32_bf16 v[22:25], v[130:133], v[186:189], v[22:25]
	s_barrier
	s_add_i32 s84, s84, 2
	s_addk_i32 s64, 0x100
	s_addk_i32 s65, 0x100
	s_cmp_gt_u32 s84, 29
	s_cbranch_scc0 .LBB0_114
	s_and_b64 vcc, exec, s[56:57]
	s_cbranch_vccz .LBB0_127
	s_barrier
	s_cmp_gt_i32 s61, 23
	s_mov_b64 s[46:47], -1
	s_cbranch_scc1 .LBB0_128

.LBB0_686:
	v_add_u32_e32 v152, 0x10000, v138
	v_add_u32_e32 v168, 0x14000, v138
	ds_read_b128 v[140:143], v152
	ds_read_b128 v[144:147], v152 offset:1024
	ds_read_b128 v[148:151], v152 offset:2048
	ds_read_b128 v[152:155], v152 offset:3072
	ds_read_b128 v[156:159], v168
	ds_read_b128 v[160:163], v168 offset:1024
	ds_read_b128 v[164:167], v168 offset:2048
	ds_read_b128 v[168:171], v168 offset:3072
	s_add_i32 s10, s33, s52
	s_add_i32 s53, s27, s52
	s_add_i32 s11, s10, 0x1000
	s_addk_i32 s53, 0x1000
	s_cmp_eq_u32 s52, 0
	s_cselect_b32 s55, s49, s11
	s_cselect_b32 s54, s50, s53
	s_or_b32 s53, s55, 0x80
	s_add_i32 s10, s10, 0x80f80
	s_mov_b32 m0, s43
	ds_read_b128 v[172:175], v139
	ds_read_b128 v[176:179], v139 offset:1024
	ds_read_b128 v[180:183], v139 offset:2048
	ds_read_b128 v[184:187], v139 offset:3072
	ds_read_b128 v[188:191], v139 offset:4096
	ds_read_b128 v[192:195], v139 offset:5120
	ds_read_b128 v[196:199], v139 offset:6144
	ds_read_b128 v[200:203], v139 offset:7168
	buffer_load_dwordx4 v134, s[4:7], s10 offen lds
	s_mov_b32 m0, s44
	s_nop 0
	buffer_load_dwordx4 v136, s[4:7], s10 offen lds
	s_waitcnt vmcnt(8)
	s_waitcnt lgkmcnt(0)
	s_barrier
	s_waitcnt lgkmcnt(7)
	v_mfma_f32_16x16x32_bf16 v[126:129], v[140:143], v[172:175], v[126:129]
	v_mfma_f32_16x16x32_bf16 v[126:129], v[144:147], v[176:179], v[126:129]
	s_waitcnt lgkmcnt(5)
	v_mfma_f32_16x16x32_bf16 v[122:125], v[152:155], v[176:179], v[122:125]
	v_mfma_f32_16x16x32_bf16 v[122:125], v[148:151], v[172:175], v[122:125]
	s_waitcnt lgkmcnt(3)
	v_mfma_f32_16x16x32_bf16 v[118:121], v[156:159], v[172:175], v[118:121]
	v_mfma_f32_16x16x32_bf16 v[118:121], v[160:163], v[176:179], v[118:121]
	s_waitcnt lgkmcnt(1)
	v_mfma_f32_16x16x32_bf16 v[114:117], v[168:171], v[176:179], v[114:117]
	v_mfma_f32_16x16x32_bf16 v[114:117], v[164:167], v[172:175], v[114:117]
	v_mfma_f32_16x16x32_bf16 v[94:97], v[164:167], v[180:183], v[94:97]
	v_mfma_f32_16x16x32_bf16 v[94:97], v[168:171], v[184:187], v[94:97]
	v_mfma_f32_16x16x32_bf16 v[102:105], v[160:163], v[184:187], v[102:105]
	v_mfma_f32_16x16x32_bf16 v[102:105], v[156:159], v[180:183], v[102:105]
	v_mfma_f32_16x16x32_bf16 v[106:109], v[148:151], v[180:183], v[106:109]
	v_mfma_f32_16x16x32_bf16 v[106:109], v[152:155], v[184:187], v[106:109]
	s_waitcnt lgkmcnt(0)
	v_mfma_f32_16x16x32_bf16 v[110:113], v[144:147], v[184:187], v[110:113]
	v_mfma_f32_16x16x32_bf16 v[110:113], v[140:143], v[180:183], v[110:113]
	v_mfma_f32_16x16x32_bf16 v[98:101], v[140:143], v[188:191], v[98:101]
	v_mfma_f32_16x16x32_bf16 v[98:101], v[144:147], v[192:195], v[98:101]
	v_mfma_f32_16x16x32_bf16 v[90:93], v[152:155], v[192:195], v[90:93]
	v_mfma_f32_16x16x32_bf16 v[90:93], v[148:151], v[188:191], v[90:93]
	v_mfma_f32_16x16x32_bf16 v[86:89], v[156:159], v[188:191], v[86:89]
	v_mfma_f32_16x16x32_bf16 v[86:89], v[160:163], v[192:195], v[86:89]
	v_mfma_f32_16x16x32_bf16 v[78:81], v[168:171], v[192:195], v[78:81]
	v_mfma_f32_16x16x32_bf16 v[78:81], v[164:167], v[188:191], v[78:81]
	v_mfma_f32_16x16x32_bf16 v[66:69], v[164:167], v[196:199], v[66:69]
	v_mfma_f32_16x16x32_bf16 v[66:69], v[168:171], v[200:203], v[66:69]
	v_mfma_f32_16x16x32_bf16 v[70:73], v[160:163], v[200:203], v[70:73]
	v_mfma_f32_16x16x32_bf16 v[70:73], v[156:159], v[196:199], v[70:73]
	v_mfma_f32_16x16x32_bf16 v[74:77], v[148:151], v[196:199], v[74:77]
	v_mfma_f32_16x16x32_bf16 v[74:77], v[152:155], v[200:203], v[74:77]
	v_mfma_f32_16x16x32_bf16 v[82:85], v[144:147], v[200:203], v[82:85]
	v_mfma_f32_16x16x32_bf16 v[82:85], v[140:143], v[196:199], v[82:85]
	s_barrier
	s_mov_b32 m0, s26
	s_mov_b32 s10, s6
	s_mov_b32 s11, s7
	ds_read_b128 v[172:175], v139 offset:16384
	ds_read_b128 v[176:179], v139 offset:17408
	ds_read_b128 v[180:183], v139 offset:18432
	ds_read_b128 v[184:187], v139 offset:19456
	ds_read_b128 v[188:191], v139 offset:20480
	ds_read_b128 v[192:195], v139 offset:21504
	ds_read_b128 v[196:199], v139 offset:22528
	ds_read_b128 v[200:203], v139 offset:23552
	buffer_load_dwordx4 v135, s[8:11], s54 offen lds
	s_mov_b32 m0, s28
	s_add_i32 s56, s54, 0x80000
	buffer_load_dwordx4 v137, s[8:11], s54 offen lds
	s_mov_b32 m0, s29
	s_nop 0
	buffer_load_dwordx4 v135, s[8:11], s56 offen lds
	s_mov_b32 m0, s30
	s_nop 0
	buffer_load_dwordx4 v137, s[8:11], s56 offen lds
	s_mov_b32 m0, s25
	s_nop 0
	buffer_load_dwordx4 v134, s[4:7], s55 offen lds
	s_mov_b32 m0, s31
	s_nop 0
	buffer_load_dwordx4 v136, s[4:7], s55 offen lds
	s_waitcnt vmcnt(8)
	s_waitcnt lgkmcnt(0)
	s_barrier
	s_waitcnt lgkmcnt(7)
	v_mfma_f32_16x16x32_bf16 v[62:65], v[140:143], v[172:175], v[62:65]
	v_mfma_f32_16x16x32_bf16 v[62:65], v[144:147], v[176:179], v[62:65]
	s_waitcnt lgkmcnt(5)
	v_mfma_f32_16x16x32_bf16 v[58:61], v[152:155], v[176:179], v[58:61]
	v_mfma_f32_16x16x32_bf16 v[58:61], v[148:151], v[172:175], v[58:61]
	s_waitcnt lgkmcnt(3)
	v_mfma_f32_16x16x32_bf16 v[54:57], v[156:159], v[172:175], v[54:57]
	v_mfma_f32_16x16x32_bf16 v[54:57], v[160:163], v[176:179], v[54:57]
	s_waitcnt lgkmcnt(1)
	v_mfma_f32_16x16x32_bf16 v[50:53], v[168:171], v[176:179], v[50:53]
	v_mfma_f32_16x16x32_bf16 v[50:53], v[164:167], v[172:175], v[50:53]
	v_mfma_f32_16x16x32_bf16 v[34:37], v[164:167], v[180:183], v[34:37]
	v_mfma_f32_16x16x32_bf16 v[34:37], v[168:171], v[184:187], v[34:37]
	v_mfma_f32_16x16x32_bf16 v[38:41], v[160:163], v[184:187], v[38:41]
	v_mfma_f32_16x16x32_bf16 v[38:41], v[156:159], v[180:183], v[38:41]
	v_mfma_f32_16x16x32_bf16 v[42:45], v[148:151], v[180:183], v[42:45]
	v_mfma_f32_16x16x32_bf16 v[42:45], v[152:155], v[184:187], v[42:45]
	s_waitcnt lgkmcnt(0)
	v_mfma_f32_16x16x32_bf16 v[46:49], v[144:147], v[184:187], v[46:49]
	v_mfma_f32_16x16x32_bf16 v[46:49], v[140:143], v[180:183], v[46:49]
	v_mfma_f32_16x16x32_bf16 v[30:33], v[140:143], v[188:191], v[30:33]
	v_mfma_f32_16x16x32_bf16 v[30:33], v[144:147], v[192:195], v[30:33]
	v_mfma_f32_16x16x32_bf16 v[26:29], v[152:155], v[192:195], v[26:29]
	v_mfma_f32_16x16x32_bf16 v[26:29], v[148:151], v[188:191], v[26:29]
	v_mfma_f32_16x16x32_bf16 v[22:25], v[156:159], v[188:191], v[22:25]
	v_mfma_f32_16x16x32_bf16 v[22:25], v[160:163], v[192:195], v[22:25]
	v_mfma_f32_16x16x32_bf16 v[18:21], v[168:171], v[192:195], v[18:21]
	v_mfma_f32_16x16x32_bf16 v[18:21], v[164:167], v[188:191], v[18:21]
	v_mfma_f32_16x16x32_bf16 v[2:5], v[164:167], v[196:199], v[2:5]
	v_mfma_f32_16x16x32_bf16 v[2:5], v[168:171], v[200:203], v[2:5]
	v_mfma_f32_16x16x32_bf16 v[6:9], v[160:163], v[200:203], v[6:9]
	v_mfma_f32_16x16x32_bf16 v[6:9], v[156:159], v[196:199], v[6:9]
	v_mfma_f32_16x16x32_bf16 v[10:13], v[148:151], v[196:199], v[10:13]
	v_mfma_f32_16x16x32_bf16 v[10:13], v[152:155], v[200:203], v[10:13]
	v_mfma_f32_16x16x32_bf16 v[14:17], v[144:147], v[200:203], v[14:17]
	v_mfma_f32_16x16x32_bf16 v[14:17], v[140:143], v[196:199], v[14:17]
	s_barrier
	v_add_u32_e32 v152, 0x18000, v138
	v_add_u32_e32 v168, 0x1c000, v138
	ds_read_b128 v[140:143], v152
	ds_read_b128 v[144:147], v152 offset:1024
	ds_read_b128 v[148:151], v152 offset:2048
	ds_read_b128 v[152:155], v152 offset:3072
	ds_read_b128 v[156:159], v168
	ds_read_b128 v[160:163], v168 offset:1024
	ds_read_b128 v[164:167], v168 offset:2048
	ds_read_b128 v[168:171], v168 offset:3072
	s_add_i32 s55, s55, 0x80000
	s_mov_b32 m0, s34
	ds_read_b128 v[172:175], v139 offset:32768
	ds_read_b128 v[176:179], v139 offset:33792
	ds_read_b128 v[180:183], v139 offset:34816
	ds_read_b128 v[184:187], v139 offset:35840
	ds_read_b128 v[188:191], v139 offset:36864
	ds_read_b128 v[192:195], v139 offset:37888
	ds_read_b128 v[196:199], v139 offset:38912
	ds_read_b128 v[200:203], v139 offset:39936
	buffer_load_dwordx4 v134, s[4:7], s55 offen lds
	s_mov_b32 m0, s35
	s_nop 0
	buffer_load_dwordx4 v136, s[4:7], s55 offen lds
	s_waitcnt vmcnt(8)
	s_waitcnt lgkmcnt(0)
	s_barrier
	s_waitcnt lgkmcnt(7)
	v_mfma_f32_16x16x32_bf16 v[126:129], v[140:143], v[172:175], v[126:129]
	v_mfma_f32_16x16x32_bf16 v[126:129], v[144:147], v[176:179], v[126:129]
	s_waitcnt lgkmcnt(5)
	v_mfma_f32_16x16x32_bf16 v[122:125], v[152:155], v[176:179], v[122:125]
	v_mfma_f32_16x16x32_bf16 v[122:125], v[148:151], v[172:175], v[122:125]
	s_waitcnt lgkmcnt(3)
	v_mfma_f32_16x16x32_bf16 v[118:121], v[156:159], v[172:175], v[118:121]
	v_mfma_f32_16x16x32_bf16 v[118:121], v[160:163], v[176:179], v[118:121]
	s_waitcnt lgkmcnt(1)
	v_mfma_f32_16x16x32_bf16 v[114:117], v[168:171], v[176:179], v[114:117]
	v_mfma_f32_16x16x32_bf16 v[114:117], v[164:167], v[172:175], v[114:117]
	v_mfma_f32_16x16x32_bf16 v[94:97], v[164:167], v[180:183], v[94:97]
	v_mfma_f32_16x16x32_bf16 v[94:97], v[168:171], v[184:187], v[94:97]
	v_mfma_f32_16x16x32_bf16 v[102:105], v[160:163], v[184:187], v[102:105]
	v_mfma_f32_16x16x32_bf16 v[102:105], v[156:159], v[180:183], v[102:105]
	v_mfma_f32_16x16x32_bf16 v[106:109], v[148:151], v[180:183], v[106:109]
	v_mfma_f32_16x16x32_bf16 v[106:109], v[152:155], v[184:187], v[106:109]
	s_waitcnt lgkmcnt(0)
	v_mfma_f32_16x16x32_bf16 v[110:113], v[144:147], v[184:187], v[110:113]
	v_mfma_f32_16x16x32_bf16 v[110:113], v[140:143], v[180:183], v[110:113]
	v_mfma_f32_16x16x32_bf16 v[98:101], v[140:143], v[188:191], v[98:101]
	v_mfma_f32_16x16x32_bf16 v[98:101], v[144:147], v[192:195], v[98:101]
	v_mfma_f32_16x16x32_bf16 v[90:93], v[152:155], v[192:195], v[90:93]
	v_mfma_f32_16x16x32_bf16 v[90:93], v[148:151], v[188:191], v[90:93]
	v_mfma_f32_16x16x32_bf16 v[86:89], v[156:159], v[188:191], v[86:89]
	v_mfma_f32_16x16x32_bf16 v[86:89], v[160:163], v[192:195], v[86:89]
	v_mfma_f32_16x16x32_bf16 v[78:81], v[168:171], v[192:195], v[78:81]
	v_mfma_f32_16x16x32_bf16 v[78:81], v[164:167], v[188:191], v[78:81]
	v_mfma_f32_16x16x32_bf16 v[66:69], v[164:167], v[196:199], v[66:69]
	v_mfma_f32_16x16x32_bf16 v[66:69], v[168:171], v[200:203], v[66:69]
	v_mfma_f32_16x16x32_bf16 v[70:73], v[160:163], v[200:203], v[70:73]
	v_mfma_f32_16x16x32_bf16 v[70:73], v[156:159], v[196:199], v[70:73]
	v_mfma_f32_16x16x32_bf16 v[74:77], v[148:151], v[196:199], v[74:77]
	v_mfma_f32_16x16x32_bf16 v[74:77], v[152:155], v[200:203], v[74:77]
	v_mfma_f32_16x16x32_bf16 v[82:85], v[144:147], v[200:203], v[82:85]
	v_mfma_f32_16x16x32_bf16 v[82:85], v[140:143], v[196:199], v[82:85]
	s_barrier
	s_mov_b32 m0, s36
	s_or_b32 s55, s54, 0x80
	ds_read_b128 v[172:175], v139 offset:49152
	ds_read_b128 v[176:179], v139 offset:50176
	ds_read_b128 v[180:183], v139 offset:51200
	ds_read_b128 v[184:187], v139 offset:52224
	ds_read_b128 v[188:191], v139 offset:53248
	ds_read_b128 v[192:195], v139 offset:54272
	ds_read_b128 v[196:199], v139 offset:55296
	ds_read_b128 v[200:203], v139 offset:56320
	buffer_load_dwordx4 v135, s[8:11], s55 offen lds
	s_mov_b32 m0, s37
	s_add_i32 s54, s54, 0x80080
	buffer_load_dwordx4 v137, s[8:11], s55 offen lds
	s_mov_b32 m0, s41
	s_nop 0
	buffer_load_dwordx4 v135, s[8:11], s54 offen lds
	s_mov_b32 m0, s42
	s_nop 0
	buffer_load_dwordx4 v137, s[8:11], s54 offen lds
	s_mov_b32 m0, s38
	s_nop 0
	buffer_load_dwordx4 v134, s[4:7], s53 offen lds
	s_mov_b32 m0, s40
	s_nop 0
	buffer_load_dwordx4 v136, s[4:7], s53 offen lds
	s_waitcnt vmcnt(8)
	s_waitcnt lgkmcnt(0)
	s_barrier
	s_waitcnt lgkmcnt(7)
	v_mfma_f32_16x16x32_bf16 v[62:65], v[140:143], v[172:175], v[62:65]
	v_mfma_f32_16x16x32_bf16 v[62:65], v[144:147], v[176:179], v[62:65]
	s_waitcnt lgkmcnt(5)
	v_mfma_f32_16x16x32_bf16 v[58:61], v[152:155], v[176:179], v[58:61]
	v_mfma_f32_16x16x32_bf16 v[58:61], v[148:151], v[172:175], v[58:61]
	s_waitcnt lgkmcnt(3)
	v_mfma_f32_16x16x32_bf16 v[54:57], v[156:159], v[172:175], v[54:57]
	v_mfma_f32_16x16x32_bf16 v[54:57], v[160:163], v[176:179], v[54:57]
	s_waitcnt lgkmcnt(1)
	v_mfma_f32_16x16x32_bf16 v[50:53], v[168:171], v[176:179], v[50:53]
	v_mfma_f32_16x16x32_bf16 v[50:53], v[164:167], v[172:175], v[50:53]
	v_mfma_f32_16x16x32_bf16 v[34:37], v[164:167], v[180:183], v[34:37]
	v_mfma_f32_16x16x32_bf16 v[34:37], v[168:171], v[184:187], v[34:37]
	v_mfma_f32_16x16x32_bf16 v[38:41], v[160:163], v[184:187], v[38:41]
	v_mfma_f32_16x16x32_bf16 v[38:41], v[156:159], v[180:183], v[38:41]
	v_mfma_f32_16x16x32_bf16 v[42:45], v[148:151], v[180:183], v[42:45]
	v_mfma_f32_16x16x32_bf16 v[42:45], v[152:155], v[184:187], v[42:45]
	s_waitcnt lgkmcnt(0)
	v_mfma_f32_16x16x32_bf16 v[46:49], v[144:147], v[184:187], v[46:49]
	v_mfma_f32_16x16x32_bf16 v[46:49], v[140:143], v[180:183], v[46:49]
	v_mfma_f32_16x16x32_bf16 v[30:33], v[140:143], v[188:191], v[30:33]
	v_mfma_f32_16x16x32_bf16 v[30:33], v[144:147], v[192:195], v[30:33]
	v_mfma_f32_16x16x32_bf16 v[26:29], v[152:155], v[192:195], v[26:29]
	v_mfma_f32_16x16x32_bf16 v[26:29], v[148:151], v[188:191], v[26:29]
	v_mfma_f32_16x16x32_bf16 v[22:25], v[156:159], v[188:191], v[22:25]
	v_mfma_f32_16x16x32_bf16 v[22:25], v[160:163], v[192:195], v[22:25]
	v_mfma_f32_16x16x32_bf16 v[18:21], v[168:171], v[192:195], v[18:21]
	v_mfma_f32_16x16x32_bf16 v[18:21], v[164:167], v[188:191], v[18:21]
	v_mfma_f32_16x16x32_bf16 v[2:5], v[164:167], v[196:199], v[2:5]
	v_mfma_f32_16x16x32_bf16 v[2:5], v[168:171], v[200:203], v[2:5]
	v_mfma_f32_16x16x32_bf16 v[6:9], v[160:163], v[200:203], v[6:9]
	v_mfma_f32_16x16x32_bf16 v[6:9], v[156:159], v[196:199], v[6:9]
	v_mfma_f32_16x16x32_bf16 v[10:13], v[148:151], v[196:199], v[10:13]
	v_mfma_f32_16x16x32_bf16 v[10:13], v[152:155], v[200:203], v[10:13]
	v_mfma_f32_16x16x32_bf16 v[14:17], v[144:147], v[200:203], v[14:17]
	v_mfma_f32_16x16x32_bf16 v[14:17], v[140:143], v[196:199], v[14:17]
	s_barrier
	s_add_i32 s51, s51, 2
	s_addk_i32 s52, 0x100
	s_cmp_gt_u32 s51, 29
	s_cbranch_scc0 .LBB0_686
	s_andn2_b64 vcc, exec, s[2:3]
	s_cbranch_vccnz .LBB0_678
	v_mov_b32_e32 v2, 0
	s_mov_b32 s14, s46
	s_mov_b32 s15, s47
	s_mov_b32 s27, s48
	s_mov_b32 s33, s13
	s_mov_b32 s45, s12
	v_mov_b32_e32 v3, v2
	v_mov_b32_e32 v4, v2
	v_mov_b32_e32 v5, v2
	v_mov_b32_e32 v6, v2
	v_mov_b32_e32 v7, v2
	v_mov_b32_e32 v8, v2
	v_mov_b32_e32 v9, v2
	v_mov_b32_e32 v18, v2
	v_mov_b32_e32 v19, v2
	v_mov_b32_e32 v20, v2
	v_mov_b32_e32 v21, v2
	v_mov_b32_e32 v22, v2
	v_mov_b32_e32 v23, v2
	v_mov_b32_e32 v24, v2
	v_mov_b32_e32 v25, v2
	v_mov_b32_e32 v34, v2
	v_mov_b32_e32 v35, v2
	v_mov_b32_e32 v36, v2
	v_mov_b32_e32 v37, v2
	v_mov_b32_e32 v38, v2
	v_mov_b32_e32 v39, v2
	v_mov_b32_e32 v40, v2
	v_mov_b32_e32 v41, v2
	v_mov_b32_e32 v50, v2
	v_mov_b32_e32 v51, v2
	v_mov_b32_e32 v52, v2
	v_mov_b32_e32 v53, v2
	v_mov_b32_e32 v54, v2
	v_mov_b32_e32 v55, v2
	v_mov_b32_e32 v56, v2
	v_mov_b32_e32 v57, v2
	v_mov_b32_e32 v10, v2
	v_mov_b32_e32 v11, v2
	v_mov_b32_e32 v12, v2
	v_mov_b32_e32 v13, v2
	v_mov_b32_e32 v14, v2
	v_mov_b32_e32 v15, v2
	v_mov_b32_e32 v16, v2
	v_mov_b32_e32 v17, v2
	v_mov_b32_e32 v26, v2
	v_mov_b32_e32 v27, v2
	v_mov_b32_e32 v28, v2
	v_mov_b32_e32 v29, v2
	v_mov_b32_e32 v30, v2
	v_mov_b32_e32 v31, v2
	v_mov_b32_e32 v32, v2
	v_mov_b32_e32 v33, v2
	v_mov_b32_e32 v42, v2
	v_mov_b32_e32 v43, v2
	v_mov_b32_e32 v44, v2
	v_mov_b32_e32 v45, v2
	v_mov_b32_e32 v46, v2
	v_mov_b32_e32 v47, v2
	v_mov_b32_e32 v48, v2
	v_mov_b32_e32 v49, v2
	v_mov_b32_e32 v58, v2
	v_mov_b32_e32 v59, v2
	v_mov_b32_e32 v60, v2
	v_mov_b32_e32 v61, v2
	v_mov_b32_e32 v62, v2
	v_mov_b32_e32 v63, v2
	v_mov_b32_e32 v64, v2
	v_mov_b32_e32 v65, v2
	v_mov_b32_e32 v66, v2
	v_mov_b32_e32 v67, v2
	v_mov_b32_e32 v68, v2
	v_mov_b32_e32 v69, v2
	v_mov_b32_e32 v70, v2
	v_mov_b32_e32 v71, v2
	v_mov_b32_e32 v72, v2
	v_mov_b32_e32 v73, v2
	v_mov_b32_e32 v78, v2
	v_mov_b32_e32 v79, v2
	v_mov_b32_e32 v80, v2
	v_mov_b32_e32 v81, v2
	v_mov_b32_e32 v86, v2
	v_mov_b32_e32 v87, v2
	v_mov_b32_e32 v88, v2
	v_mov_b32_e32 v89, v2
	v_mov_b32_e32 v94, v2
	v_mov_b32_e32 v95, v2
	v_mov_b32_e32 v96, v2
	v_mov_b32_e32 v97, v2
	v_mov_b32_e32 v102, v2
	v_mov_b32_e32 v103, v2
	v_mov_b32_e32 v104, v2
	v_mov_b32_e32 v105, v2
	v_mov_b32_e32 v114, v2
	v_mov_b32_e32 v115, v2
	v_mov_b32_e32 v116, v2
	v_mov_b32_e32 v117, v2
	v_mov_b32_e32 v118, v2
	v_mov_b32_e32 v119, v2
	v_mov_b32_e32 v120, v2
	v_mov_b32_e32 v121, v2
	v_mov_b32_e32 v74, v2
	v_mov_b32_e32 v75, v2
	v_mov_b32_e32 v76, v2
	v_mov_b32_e32 v77, v2
	v_mov_b32_e32 v82, v2
	v_mov_b32_e32 v83, v2
	v_mov_b32_e32 v84, v2
	v_mov_b32_e32 v85, v2
	v_mov_b32_e32 v90, v2
	v_mov_b32_e32 v91, v2
	v_mov_b32_e32 v92, v2
	v_mov_b32_e32 v93, v2
	v_mov_b32_e32 v98, v2
	v_mov_b32_e32 v99, v2
	v_mov_b32_e32 v100, v2
	v_mov_b32_e32 v101, v2
	v_mov_b32_e32 v106, v2
	v_mov_b32_e32 v107, v2
	v_mov_b32_e32 v108, v2
	v_mov_b32_e32 v109, v2
	v_mov_b32_e32 v110, v2
	v_mov_b32_e32 v111, v2
	v_mov_b32_e32 v112, v2
	v_mov_b32_e32 v113, v2
	v_mov_b32_e32 v122, v2
	v_mov_b32_e32 v123, v2
	v_mov_b32_e32 v124, v2
	v_mov_b32_e32 v125, v2
	v_mov_b32_e32 v126, v2
	v_mov_b32_e32 v127, v2
	v_mov_b32_e32 v128, v2
	v_mov_b32_e32 v129, v2
	s_branch .LBB0_678

.LBB0_907:
	v_add_u32_e32 v166, 0x10000, v179
	ds_read_b128 v[162:165], v166
	ds_read_b128 v[182:185], v166 offset:1024
	ds_read_b128 v[186:189], v166 offset:2048
	ds_read_b128 v[190:193], v166 offset:3072
	v_add_u32_e32 v166, 0x14000, v179
	ds_read_b128 v[194:197], v166
	ds_read_b128 v[198:201], v166 offset:1024
	ds_read_b128 v[202:205], v166 offset:2048
	ds_read_b128 v[206:209], v166 offset:3072
	s_add_i32 s10, s45, s64
	s_add_i32 s26, s40, s64
	s_add_i32 s11, s10, 0x1000
	s_addk_i32 s26, 0x1000
	s_cmp_eq_u32 s64, 0
	s_cselect_b32 s29, s62, s11
	s_cselect_b32 s27, s63, s26
	s_add_i32 s26, s29, 0x80
	s_add_i32 s28, s27, 0x80
	s_add_i32 s10, s10, 0x80f80
	s_mov_b32 m0, s55
	ds_read_b128 v[210:213], v180
	ds_read_b128 v[214:217], v180 offset:1024
	ds_read_b128 v[218:221], v180 offset:2048
	ds_read_b128 v[222:225], v180 offset:3072
	ds_read_b128 v[226:229], v180 offset:4096
	ds_read_b128 v[230:233], v180 offset:5120
	ds_read_b128 v[234:237], v180 offset:6144
	ds_read_b128 v[238:241], v180 offset:7168
	buffer_load_dwordx4 v1, s[4:7], s10 offen lds
	s_mov_b32 m0, s56
	s_nop 0
	buffer_load_dwordx4 v175, s[4:7], s10 offen lds
	s_waitcnt vmcnt(8)
	s_waitcnt lgkmcnt(0)
	s_barrier
	s_waitcnt lgkmcnt(7)
	v_mfma_f32_16x16x32_bf16 v[126:129], v[162:165], v[210:213], v[126:129]
	v_mfma_f32_16x16x32_bf16 v[126:129], v[182:185], v[214:217], v[126:129]
	s_waitcnt lgkmcnt(5)
	v_mfma_f32_16x16x32_bf16 v[122:125], v[190:193], v[214:217], v[122:125]
	v_mfma_f32_16x16x32_bf16 v[122:125], v[186:189], v[210:213], v[122:125]
	s_waitcnt lgkmcnt(3)
	v_mfma_f32_16x16x32_bf16 v[94:97], v[194:197], v[210:213], v[94:97]
	v_mfma_f32_16x16x32_bf16 v[94:97], v[198:201], v[214:217], v[94:97]
	s_waitcnt lgkmcnt(1)
	v_mfma_f32_16x16x32_bf16 v[90:93], v[206:209], v[214:217], v[90:93]
	v_mfma_f32_16x16x32_bf16 v[90:93], v[202:205], v[210:213], v[90:93]
	v_mfma_f32_16x16x32_bf16 v[82:85], v[202:205], v[218:221], v[82:85]
	v_mfma_f32_16x16x32_bf16 v[82:85], v[206:209], v[222:225], v[82:85]
	v_mfma_f32_16x16x32_bf16 v[86:89], v[198:201], v[222:225], v[86:89]
	v_mfma_f32_16x16x32_bf16 v[86:89], v[194:197], v[218:221], v[86:89]
	v_mfma_f32_16x16x32_bf16 v[114:117], v[186:189], v[218:221], v[114:117]
	v_mfma_f32_16x16x32_bf16 v[114:117], v[190:193], v[222:225], v[114:117]
	s_waitcnt lgkmcnt(0)
	v_mfma_f32_16x16x32_bf16 v[118:121], v[182:185], v[222:225], v[118:121]
	v_mfma_f32_16x16x32_bf16 v[118:121], v[162:165], v[218:221], v[118:121]
	v_mfma_f32_16x16x32_bf16 v[110:113], v[162:165], v[226:229], v[110:113]
	v_mfma_f32_16x16x32_bf16 v[110:113], v[182:185], v[230:233], v[110:113]
	v_mfma_f32_16x16x32_bf16 v[106:109], v[190:193], v[230:233], v[106:109]
	v_mfma_f32_16x16x32_bf16 v[106:109], v[186:189], v[226:229], v[106:109]
	v_mfma_f32_16x16x32_bf16 v[78:81], v[194:197], v[226:229], v[78:81]
	v_mfma_f32_16x16x32_bf16 v[78:81], v[198:201], v[230:233], v[78:81]
	v_mfma_f32_16x16x32_bf16 v[74:77], v[206:209], v[230:233], v[74:77]
	v_mfma_f32_16x16x32_bf16 v[74:77], v[202:205], v[226:229], v[74:77]
	v_mfma_f32_16x16x32_bf16 v[66:69], v[202:205], v[234:237], v[66:69]
	v_mfma_f32_16x16x32_bf16 v[66:69], v[206:209], v[238:241], v[66:69]
	v_mfma_f32_16x16x32_bf16 v[70:73], v[198:201], v[238:241], v[70:73]
	v_mfma_f32_16x16x32_bf16 v[70:73], v[194:197], v[234:237], v[70:73]
	v_mfma_f32_16x16x32_bf16 v[98:101], v[186:189], v[234:237], v[98:101]
	v_mfma_f32_16x16x32_bf16 v[98:101], v[190:193], v[238:241], v[98:101]
	v_mfma_f32_16x16x32_bf16 v[102:105], v[182:185], v[238:241], v[102:105]
	v_mfma_f32_16x16x32_bf16 v[102:105], v[162:165], v[234:237], v[102:105]
	s_barrier
	s_mov_b32 m0, s37
	s_mov_b32 s10, s6
	s_mov_b32 s11, s7
	ds_read_b128 v[210:213], v180 offset:16384
	ds_read_b128 v[214:217], v180 offset:17408
	ds_read_b128 v[218:221], v180 offset:18432
	ds_read_b128 v[222:225], v180 offset:19456
	ds_read_b128 v[226:229], v180 offset:20480
	ds_read_b128 v[230:233], v180 offset:21504
	ds_read_b128 v[234:237], v180 offset:22528
	ds_read_b128 v[238:241], v180 offset:23552
	buffer_load_dwordx4 v174, s[8:11], s27 offen lds
	s_mov_b32 m0, s38
	s_add_i32 s66, s27, 0x80000
	buffer_load_dwordx4 v176, s[8:11], s27 offen lds
	s_mov_b32 m0, s39
	s_nop 0
	buffer_load_dwordx4 v174, s[8:11], s66 offen lds
	s_mov_b32 m0, s41
	s_nop 0
	buffer_load_dwordx4 v176, s[8:11], s66 offen lds
	s_mov_b32 m0, s36
	s_nop 0
	buffer_load_dwordx4 v1, s[4:7], s29 offen lds
	s_mov_b32 m0, s42
	s_nop 0
	buffer_load_dwordx4 v175, s[4:7], s29 offen lds
	s_waitcnt vmcnt(8)
	s_waitcnt lgkmcnt(0)
	s_barrier
	s_waitcnt lgkmcnt(7)
	v_mfma_f32_16x16x32_bf16 v[62:65], v[162:165], v[210:213], v[62:65]
	v_mfma_f32_16x16x32_bf16 v[62:65], v[182:185], v[214:217], v[62:65]
	s_waitcnt lgkmcnt(5)
	v_mfma_f32_16x16x32_bf16 v[58:61], v[190:193], v[214:217], v[58:61]
	v_mfma_f32_16x16x32_bf16 v[58:61], v[186:189], v[210:213], v[58:61]
	s_waitcnt lgkmcnt(3)
	v_mfma_f32_16x16x32_bf16 v[30:33], v[194:197], v[210:213], v[30:33]
	v_mfma_f32_16x16x32_bf16 v[30:33], v[198:201], v[214:217], v[30:33]
	s_waitcnt lgkmcnt(1)
	v_mfma_f32_16x16x32_bf16 v[26:29], v[206:209], v[214:217], v[26:29]
	v_mfma_f32_16x16x32_bf16 v[26:29], v[202:205], v[210:213], v[26:29]
	v_mfma_f32_16x16x32_bf16 v[18:21], v[202:205], v[218:221], v[18:21]
	v_mfma_f32_16x16x32_bf16 v[18:21], v[206:209], v[222:225], v[18:21]
	v_mfma_f32_16x16x32_bf16 v[22:25], v[198:201], v[222:225], v[22:25]
	v_mfma_f32_16x16x32_bf16 v[22:25], v[194:197], v[218:221], v[22:25]
	v_mfma_f32_16x16x32_bf16 v[50:53], v[186:189], v[218:221], v[50:53]
	v_mfma_f32_16x16x32_bf16 v[50:53], v[190:193], v[222:225], v[50:53]
	s_waitcnt lgkmcnt(0)
	v_mfma_f32_16x16x32_bf16 v[54:57], v[182:185], v[222:225], v[54:57]
	v_mfma_f32_16x16x32_bf16 v[54:57], v[162:165], v[218:221], v[54:57]
	v_mfma_f32_16x16x32_bf16 v[46:49], v[162:165], v[226:229], v[46:49]
	v_mfma_f32_16x16x32_bf16 v[46:49], v[182:185], v[230:233], v[46:49]
	v_mfma_f32_16x16x32_bf16 v[42:45], v[190:193], v[230:233], v[42:45]
	v_mfma_f32_16x16x32_bf16 v[42:45], v[186:189], v[226:229], v[42:45]
	v_mfma_f32_16x16x32_bf16 v[14:17], v[194:197], v[226:229], v[14:17]
	v_mfma_f32_16x16x32_bf16 v[14:17], v[198:201], v[230:233], v[14:17]
	v_mfma_f32_16x16x32_bf16 v[10:13], v[206:209], v[230:233], v[10:13]
	v_mfma_f32_16x16x32_bf16 v[10:13], v[202:205], v[226:229], v[10:13]
	v_mfma_f32_16x16x32_bf16 v[2:5], v[202:205], v[234:237], v[2:5]
	v_mfma_f32_16x16x32_bf16 v[2:5], v[206:209], v[238:241], v[2:5]
	v_mfma_f32_16x16x32_bf16 v[6:9], v[198:201], v[238:241], v[6:9]
	v_mfma_f32_16x16x32_bf16 v[6:9], v[194:197], v[234:237], v[6:9]
	v_mfma_f32_16x16x32_bf16 v[34:37], v[186:189], v[234:237], v[34:37]
	v_mfma_f32_16x16x32_bf16 v[34:37], v[190:193], v[238:241], v[34:37]
	v_mfma_f32_16x16x32_bf16 v[38:41], v[182:185], v[238:241], v[38:41]
	v_mfma_f32_16x16x32_bf16 v[38:41], v[162:165], v[234:237], v[38:41]
	s_barrier
	v_add_u32_e32 v166, 0x18000, v179
	ds_read_b128 v[162:165], v166
	ds_read_b128 v[182:185], v166 offset:1024
	ds_read_b128 v[186:189], v166 offset:2048
	ds_read_b128 v[190:193], v166 offset:3072
	v_add_u32_e32 v166, 0x1c000, v179
	ds_read_b128 v[194:197], v166
	ds_read_b128 v[198:201], v166 offset:1024
	ds_read_b128 v[202:205], v166 offset:2048
	ds_read_b128 v[206:209], v166 offset:3072
	s_add_i32 s29, s29, 0x80000
	s_mov_b32 m0, s43
	ds_read_b128 v[210:213], v180 offset:32768
	ds_read_b128 v[214:217], v180 offset:33792
	ds_read_b128 v[218:221], v180 offset:34816
	ds_read_b128 v[222:225], v180 offset:35840
	ds_read_b128 v[226:229], v180 offset:36864
	ds_read_b128 v[230:233], v180 offset:37888
	ds_read_b128 v[234:237], v180 offset:38912
	ds_read_b128 v[238:241], v180 offset:39936
	buffer_load_dwordx4 v1, s[4:7], s29 offen lds
	s_mov_b32 m0, s44
	s_nop 0
	buffer_load_dwordx4 v175, s[4:7], s29 offen lds
	s_waitcnt vmcnt(8)
	s_waitcnt lgkmcnt(0)
	s_barrier
	s_waitcnt lgkmcnt(7)
	v_mfma_f32_16x16x32_bf16 v[126:129], v[162:165], v[210:213], v[126:129]
	v_mfma_f32_16x16x32_bf16 v[126:129], v[182:185], v[214:217], v[126:129]
	s_waitcnt lgkmcnt(5)
	v_mfma_f32_16x16x32_bf16 v[122:125], v[190:193], v[214:217], v[122:125]
	v_mfma_f32_16x16x32_bf16 v[122:125], v[186:189], v[210:213], v[122:125]
	s_waitcnt lgkmcnt(3)
	v_mfma_f32_16x16x32_bf16 v[94:97], v[194:197], v[210:213], v[94:97]
	v_mfma_f32_16x16x32_bf16 v[94:97], v[198:201], v[214:217], v[94:97]
	s_waitcnt lgkmcnt(1)
	v_mfma_f32_16x16x32_bf16 v[90:93], v[206:209], v[214:217], v[90:93]
	v_mfma_f32_16x16x32_bf16 v[90:93], v[202:205], v[210:213], v[90:93]
	v_mfma_f32_16x16x32_bf16 v[82:85], v[202:205], v[218:221], v[82:85]
	v_mfma_f32_16x16x32_bf16 v[82:85], v[206:209], v[222:225], v[82:85]
	v_mfma_f32_16x16x32_bf16 v[86:89], v[198:201], v[222:225], v[86:89]
	v_mfma_f32_16x16x32_bf16 v[86:89], v[194:197], v[218:221], v[86:89]
	v_mfma_f32_16x16x32_bf16 v[114:117], v[186:189], v[218:221], v[114:117]
	v_mfma_f32_16x16x32_bf16 v[114:117], v[190:193], v[222:225], v[114:117]
	s_waitcnt lgkmcnt(0)
	v_mfma_f32_16x16x32_bf16 v[118:121], v[182:185], v[222:225], v[118:121]
	v_mfma_f32_16x16x32_bf16 v[118:121], v[162:165], v[218:221], v[118:121]
	v_mfma_f32_16x16x32_bf16 v[110:113], v[162:165], v[226:229], v[110:113]
	v_mfma_f32_16x16x32_bf16 v[110:113], v[182:185], v[230:233], v[110:113]
	v_mfma_f32_16x16x32_bf16 v[106:109], v[190:193], v[230:233], v[106:109]
	v_mfma_f32_16x16x32_bf16 v[106:109], v[186:189], v[226:229], v[106:109]
	v_mfma_f32_16x16x32_bf16 v[78:81], v[194:197], v[226:229], v[78:81]
	v_mfma_f32_16x16x32_bf16 v[78:81], v[198:201], v[230:233], v[78:81]
	v_mfma_f32_16x16x32_bf16 v[74:77], v[206:209], v[230:233], v[74:77]
	v_mfma_f32_16x16x32_bf16 v[74:77], v[202:205], v[226:229], v[74:77]
	v_mfma_f32_16x16x32_bf16 v[66:69], v[202:205], v[234:237], v[66:69]
	v_mfma_f32_16x16x32_bf16 v[66:69], v[206:209], v[238:241], v[66:69]
	v_mfma_f32_16x16x32_bf16 v[70:73], v[198:201], v[238:241], v[70:73]
	v_mfma_f32_16x16x32_bf16 v[70:73], v[194:197], v[234:237], v[70:73]
	v_mfma_f32_16x16x32_bf16 v[98:101], v[186:189], v[234:237], v[98:101]
	v_mfma_f32_16x16x32_bf16 v[98:101], v[190:193], v[238:241], v[98:101]
	v_mfma_f32_16x16x32_bf16 v[102:105], v[182:185], v[238:241], v[102:105]
	v_mfma_f32_16x16x32_bf16 v[102:105], v[162:165], v[234:237], v[102:105]
	s_barrier
	s_mov_b32 m0, s49
	ds_read_b128 v[210:213], v180 offset:49152
	ds_read_b128 v[214:217], v180 offset:50176
	ds_read_b128 v[218:221], v180 offset:51200
	ds_read_b128 v[222:225], v180 offset:52224
	ds_read_b128 v[226:229], v180 offset:53248
	ds_read_b128 v[230:233], v180 offset:54272
	ds_read_b128 v[234:237], v180 offset:55296
	ds_read_b128 v[238:241], v180 offset:56320
	buffer_load_dwordx4 v174, s[8:11], s28 offen lds
	s_mov_b32 m0, s50
	s_add_i32 s27, s27, 0x80080
	buffer_load_dwordx4 v176, s[8:11], s28 offen lds
	s_mov_b32 m0, s53
	s_nop 0
	buffer_load_dwordx4 v174, s[8:11], s27 offen lds
	s_mov_b32 m0, s54
	s_nop 0
	buffer_load_dwordx4 v176, s[8:11], s27 offen lds
	s_mov_b32 m0, s51
	s_nop 0
	buffer_load_dwordx4 v1, s[4:7], s26 offen lds
	s_mov_b32 m0, s52
	s_nop 0
	buffer_load_dwordx4 v175, s[4:7], s26 offen lds
	s_waitcnt vmcnt(8)
	s_waitcnt lgkmcnt(0)
	s_barrier
	s_waitcnt lgkmcnt(7)
	v_mfma_f32_16x16x32_bf16 v[62:65], v[162:165], v[210:213], v[62:65]
	v_mfma_f32_16x16x32_bf16 v[62:65], v[182:185], v[214:217], v[62:65]
	s_waitcnt lgkmcnt(5)
	v_mfma_f32_16x16x32_bf16 v[58:61], v[190:193], v[214:217], v[58:61]
	v_mfma_f32_16x16x32_bf16 v[58:61], v[186:189], v[210:213], v[58:61]
	s_waitcnt lgkmcnt(3)
	v_mfma_f32_16x16x32_bf16 v[30:33], v[194:197], v[210:213], v[30:33]
	v_mfma_f32_16x16x32_bf16 v[30:33], v[198:201], v[214:217], v[30:33]
	s_waitcnt lgkmcnt(1)
	v_mfma_f32_16x16x32_bf16 v[26:29], v[206:209], v[214:217], v[26:29]
	v_mfma_f32_16x16x32_bf16 v[26:29], v[202:205], v[210:213], v[26:29]
	v_mfma_f32_16x16x32_bf16 v[18:21], v[202:205], v[218:221], v[18:21]
	v_mfma_f32_16x16x32_bf16 v[18:21], v[206:209], v[222:225], v[18:21]
	v_mfma_f32_16x16x32_bf16 v[22:25], v[198:201], v[222:225], v[22:25]
	v_mfma_f32_16x16x32_bf16 v[22:25], v[194:197], v[218:221], v[22:25]
	v_mfma_f32_16x16x32_bf16 v[50:53], v[186:189], v[218:221], v[50:53]
	v_mfma_f32_16x16x32_bf16 v[50:53], v[190:193], v[222:225], v[50:53]
	s_waitcnt lgkmcnt(0)
	v_mfma_f32_16x16x32_bf16 v[54:57], v[182:185], v[222:225], v[54:57]
	v_mfma_f32_16x16x32_bf16 v[54:57], v[162:165], v[218:221], v[54:57]
	v_mfma_f32_16x16x32_bf16 v[46:49], v[162:165], v[226:229], v[46:49]
	v_mfma_f32_16x16x32_bf16 v[46:49], v[182:185], v[230:233], v[46:49]
	v_mfma_f32_16x16x32_bf16 v[42:45], v[190:193], v[230:233], v[42:45]
	v_mfma_f32_16x16x32_bf16 v[42:45], v[186:189], v[226:229], v[42:45]
	v_mfma_f32_16x16x32_bf16 v[14:17], v[194:197], v[226:229], v[14:17]
	v_mfma_f32_16x16x32_bf16 v[14:17], v[198:201], v[230:233], v[14:17]
	v_mfma_f32_16x16x32_bf16 v[10:13], v[206:209], v[230:233], v[10:13]
	v_mfma_f32_16x16x32_bf16 v[10:13], v[202:205], v[226:229], v[10:13]
	v_mfma_f32_16x16x32_bf16 v[2:5], v[202:205], v[234:237], v[2:5]
	v_mfma_f32_16x16x32_bf16 v[2:5], v[206:209], v[238:241], v[2:5]
	v_mfma_f32_16x16x32_bf16 v[6:9], v[198:201], v[238:241], v[6:9]
	v_mfma_f32_16x16x32_bf16 v[6:9], v[194:197], v[234:237], v[6:9]
	v_mfma_f32_16x16x32_bf16 v[34:37], v[186:189], v[234:237], v[34:37]
	v_mfma_f32_16x16x32_bf16 v[34:37], v[190:193], v[238:241], v[34:37]
	v_mfma_f32_16x16x32_bf16 v[38:41], v[182:185], v[238:241], v[38:41]
	v_mfma_f32_16x16x32_bf16 v[38:41], v[162:165], v[234:237], v[38:41]
	s_barrier
	s_add_i32 s10, s65, 2
	s_addk_i32 s64, 0x100
	s_cmp_gt_u32 s65, 29
	s_cbranch_scc1 .LBB0_910
	s_mov_b32 s65, s10
	s_branch .LBB0_869

.LBB0_1029:
	v_add_u32_e32 v152, 0x10000, v138
	v_add_u32_e32 v168, 0x14000, v138
	ds_read_b128 v[140:143], v152
	ds_read_b128 v[144:147], v152 offset:1024
	ds_read_b128 v[148:151], v152 offset:2048
	ds_read_b128 v[152:155], v152 offset:3072
	ds_read_b128 v[156:159], v168
	ds_read_b128 v[160:163], v168 offset:1024
	ds_read_b128 v[164:167], v168 offset:2048
	ds_read_b128 v[168:171], v168 offset:3072
	s_add_i32 s10, s30, s50
	s_add_i32 s51, s25, s50
	s_add_i32 s11, s10, 0x4000
	s_addk_i32 s51, 0x4000
	s_cmp_eq_u32 s50, 0
	s_cselect_b32 s53, s47, s11
	s_cselect_b32 s52, s48, s51
	s_or_b32 s51, s53, 0x80
	s_add_i32 s10, s10, 0x203f80
	s_mov_b32 m0, s41
	ds_read_b128 v[172:175], v139
	ds_read_b128 v[176:179], v139 offset:1024
	ds_read_b128 v[180:183], v139 offset:2048
	ds_read_b128 v[184:187], v139 offset:3072
	ds_read_b128 v[188:191], v139 offset:4096
	ds_read_b128 v[192:195], v139 offset:5120
	ds_read_b128 v[196:199], v139 offset:6144
	ds_read_b128 v[200:203], v139 offset:7168
	buffer_load_dwordx4 v134, s[4:7], s10 offen lds
	s_mov_b32 m0, s42
	s_nop 0
	buffer_load_dwordx4 v136, s[4:7], s10 offen lds
	s_waitcnt vmcnt(8)
	s_waitcnt lgkmcnt(0)
	s_barrier
	s_waitcnt lgkmcnt(7)
	v_mfma_f32_16x16x32_bf16 v[126:129], v[140:143], v[172:175], v[126:129]
	v_mfma_f32_16x16x32_bf16 v[126:129], v[144:147], v[176:179], v[126:129]
	s_waitcnt lgkmcnt(5)
	v_mfma_f32_16x16x32_bf16 v[122:125], v[152:155], v[176:179], v[122:125]
	v_mfma_f32_16x16x32_bf16 v[122:125], v[148:151], v[172:175], v[122:125]
	s_waitcnt lgkmcnt(3)
	v_mfma_f32_16x16x32_bf16 v[118:121], v[156:159], v[172:175], v[118:121]
	v_mfma_f32_16x16x32_bf16 v[118:121], v[160:163], v[176:179], v[118:121]
	s_waitcnt lgkmcnt(1)
	v_mfma_f32_16x16x32_bf16 v[110:113], v[168:171], v[176:179], v[110:113]
	v_mfma_f32_16x16x32_bf16 v[110:113], v[164:167], v[172:175], v[110:113]
	v_mfma_f32_16x16x32_bf16 v[94:97], v[164:167], v[180:183], v[94:97]
	v_mfma_f32_16x16x32_bf16 v[94:97], v[168:171], v[184:187], v[94:97]
	v_mfma_f32_16x16x32_bf16 v[102:105], v[160:163], v[184:187], v[102:105]
	v_mfma_f32_16x16x32_bf16 v[102:105], v[156:159], v[180:183], v[102:105]
	v_mfma_f32_16x16x32_bf16 v[106:109], v[148:151], v[180:183], v[106:109]
	v_mfma_f32_16x16x32_bf16 v[106:109], v[152:155], v[184:187], v[106:109]
	s_waitcnt lgkmcnt(0)
	v_mfma_f32_16x16x32_bf16 v[114:117], v[144:147], v[184:187], v[114:117]
	v_mfma_f32_16x16x32_bf16 v[114:117], v[140:143], v[180:183], v[114:117]
	v_mfma_f32_16x16x32_bf16 v[98:101], v[140:143], v[188:191], v[98:101]
	v_mfma_f32_16x16x32_bf16 v[98:101], v[144:147], v[192:195], v[98:101]
	v_mfma_f32_16x16x32_bf16 v[90:93], v[152:155], v[192:195], v[90:93]
	v_mfma_f32_16x16x32_bf16 v[90:93], v[148:151], v[188:191], v[90:93]
	v_mfma_f32_16x16x32_bf16 v[86:89], v[156:159], v[188:191], v[86:89]
	v_mfma_f32_16x16x32_bf16 v[86:89], v[160:163], v[192:195], v[86:89]
	v_mfma_f32_16x16x32_bf16 v[78:81], v[168:171], v[192:195], v[78:81]
	v_mfma_f32_16x16x32_bf16 v[78:81], v[164:167], v[188:191], v[78:81]
	v_mfma_f32_16x16x32_bf16 v[66:69], v[164:167], v[196:199], v[66:69]
	v_mfma_f32_16x16x32_bf16 v[66:69], v[168:171], v[200:203], v[66:69]
	v_mfma_f32_16x16x32_bf16 v[70:73], v[160:163], v[200:203], v[70:73]
	v_mfma_f32_16x16x32_bf16 v[70:73], v[156:159], v[196:199], v[70:73]
	v_mfma_f32_16x16x32_bf16 v[74:77], v[148:151], v[196:199], v[74:77]
	v_mfma_f32_16x16x32_bf16 v[74:77], v[152:155], v[200:203], v[74:77]
	v_mfma_f32_16x16x32_bf16 v[82:85], v[144:147], v[200:203], v[82:85]
	v_mfma_f32_16x16x32_bf16 v[82:85], v[140:143], v[196:199], v[82:85]
	s_barrier
	s_mov_b32 m0, s24
	s_mov_b32 s10, s6
	s_mov_b32 s11, s7
	ds_read_b128 v[172:175], v139 offset:16384
	ds_read_b128 v[176:179], v139 offset:17408
	ds_read_b128 v[180:183], v139 offset:18432
	ds_read_b128 v[184:187], v139 offset:19456
	ds_read_b128 v[188:191], v139 offset:20480
	ds_read_b128 v[192:195], v139 offset:21504
	ds_read_b128 v[196:199], v139 offset:22528
	ds_read_b128 v[200:203], v139 offset:23552
	buffer_load_dwordx4 v135, s[8:11], s52 offen lds
	s_mov_b32 m0, s26
	s_add_i32 s54, s52, 0x200000
	buffer_load_dwordx4 v137, s[8:11], s52 offen lds
	s_mov_b32 m0, s27
	s_nop 0
	buffer_load_dwordx4 v135, s[8:11], s54 offen lds
	s_mov_b32 m0, s28
	s_nop 0
	buffer_load_dwordx4 v137, s[8:11], s54 offen lds
	s_mov_b32 m0, s23
	s_nop 0
	buffer_load_dwordx4 v134, s[4:7], s53 offen lds
	s_mov_b32 m0, s29
	s_nop 0
	buffer_load_dwordx4 v136, s[4:7], s53 offen lds
	s_waitcnt vmcnt(8)
	s_waitcnt lgkmcnt(0)
	s_barrier
	s_waitcnt lgkmcnt(7)
	v_mfma_f32_16x16x32_bf16 v[62:65], v[140:143], v[172:175], v[62:65]
	v_mfma_f32_16x16x32_bf16 v[62:65], v[144:147], v[176:179], v[62:65]
	s_waitcnt lgkmcnt(5)
	v_mfma_f32_16x16x32_bf16 v[58:61], v[152:155], v[176:179], v[58:61]
	v_mfma_f32_16x16x32_bf16 v[58:61], v[148:151], v[172:175], v[58:61]
	s_waitcnt lgkmcnt(3)
	v_mfma_f32_16x16x32_bf16 v[54:57], v[156:159], v[172:175], v[54:57]
	v_mfma_f32_16x16x32_bf16 v[54:57], v[160:163], v[176:179], v[54:57]
	s_waitcnt lgkmcnt(1)
	v_mfma_f32_16x16x32_bf16 v[46:49], v[168:171], v[176:179], v[46:49]
	v_mfma_f32_16x16x32_bf16 v[46:49], v[164:167], v[172:175], v[46:49]
	v_mfma_f32_16x16x32_bf16 v[30:33], v[164:167], v[180:183], v[30:33]
	v_mfma_f32_16x16x32_bf16 v[30:33], v[168:171], v[184:187], v[30:33]
	v_mfma_f32_16x16x32_bf16 v[38:41], v[160:163], v[184:187], v[38:41]
	v_mfma_f32_16x16x32_bf16 v[38:41], v[156:159], v[180:183], v[38:41]
	v_mfma_f32_16x16x32_bf16 v[42:45], v[148:151], v[180:183], v[42:45]
	v_mfma_f32_16x16x32_bf16 v[42:45], v[152:155], v[184:187], v[42:45]
	s_waitcnt lgkmcnt(0)
	v_mfma_f32_16x16x32_bf16 v[50:53], v[144:147], v[184:187], v[50:53]
	v_mfma_f32_16x16x32_bf16 v[50:53], v[140:143], v[180:183], v[50:53]
	v_mfma_f32_16x16x32_bf16 v[34:37], v[140:143], v[188:191], v[34:37]
	v_mfma_f32_16x16x32_bf16 v[34:37], v[144:147], v[192:195], v[34:37]
	v_mfma_f32_16x16x32_bf16 v[26:29], v[152:155], v[192:195], v[26:29]
	v_mfma_f32_16x16x32_bf16 v[26:29], v[148:151], v[188:191], v[26:29]
	v_mfma_f32_16x16x32_bf16 v[22:25], v[156:159], v[188:191], v[22:25]
	v_mfma_f32_16x16x32_bf16 v[22:25], v[160:163], v[192:195], v[22:25]
	v_mfma_f32_16x16x32_bf16 v[14:17], v[168:171], v[192:195], v[14:17]
	v_mfma_f32_16x16x32_bf16 v[14:17], v[164:167], v[188:191], v[14:17]
	v_mfma_f32_16x16x32_bf16 v[2:5], v[164:167], v[196:199], v[2:5]
	v_mfma_f32_16x16x32_bf16 v[2:5], v[168:171], v[200:203], v[2:5]
	v_mfma_f32_16x16x32_bf16 v[6:9], v[160:163], v[200:203], v[6:9]
	v_mfma_f32_16x16x32_bf16 v[6:9], v[156:159], v[196:199], v[6:9]
	v_mfma_f32_16x16x32_bf16 v[10:13], v[148:151], v[196:199], v[10:13]
	v_mfma_f32_16x16x32_bf16 v[10:13], v[152:155], v[200:203], v[10:13]
	v_mfma_f32_16x16x32_bf16 v[18:21], v[144:147], v[200:203], v[18:21]
	v_mfma_f32_16x16x32_bf16 v[18:21], v[140:143], v[196:199], v[18:21]
	s_barrier
	v_add_u32_e32 v152, 0x18000, v138
	v_add_u32_e32 v168, 0x1c000, v138
	ds_read_b128 v[140:143], v152
	ds_read_b128 v[144:147], v152 offset:1024
	ds_read_b128 v[148:151], v152 offset:2048
	ds_read_b128 v[152:155], v152 offset:3072
	ds_read_b128 v[156:159], v168
	ds_read_b128 v[160:163], v168 offset:1024
	ds_read_b128 v[164:167], v168 offset:2048
	ds_read_b128 v[168:171], v168 offset:3072
	s_add_i32 s53, s53, 0x200000
	s_mov_b32 m0, s31
	ds_read_b128 v[172:175], v139 offset:32768
	ds_read_b128 v[176:179], v139 offset:33792
	ds_read_b128 v[180:183], v139 offset:34816
	ds_read_b128 v[184:187], v139 offset:35840
	ds_read_b128 v[188:191], v139 offset:36864
	ds_read_b128 v[192:195], v139 offset:37888
	ds_read_b128 v[196:199], v139 offset:38912
	ds_read_b128 v[200:203], v139 offset:39936
	buffer_load_dwordx4 v134, s[4:7], s53 offen lds
	s_mov_b32 m0, s33
	s_nop 0
	buffer_load_dwordx4 v136, s[4:7], s53 offen lds
	s_waitcnt vmcnt(8)
	s_waitcnt lgkmcnt(0)
	s_barrier
	s_waitcnt lgkmcnt(7)
	v_mfma_f32_16x16x32_bf16 v[126:129], v[140:143], v[172:175], v[126:129]
	v_mfma_f32_16x16x32_bf16 v[126:129], v[144:147], v[176:179], v[126:129]
	s_waitcnt lgkmcnt(5)
	v_mfma_f32_16x16x32_bf16 v[122:125], v[152:155], v[176:179], v[122:125]
	v_mfma_f32_16x16x32_bf16 v[122:125], v[148:151], v[172:175], v[122:125]
	s_waitcnt lgkmcnt(3)
	v_mfma_f32_16x16x32_bf16 v[118:121], v[156:159], v[172:175], v[118:121]
	v_mfma_f32_16x16x32_bf16 v[118:121], v[160:163], v[176:179], v[118:121]
	s_waitcnt lgkmcnt(1)
	v_mfma_f32_16x16x32_bf16 v[110:113], v[168:171], v[176:179], v[110:113]
	v_mfma_f32_16x16x32_bf16 v[110:113], v[164:167], v[172:175], v[110:113]
	v_mfma_f32_16x16x32_bf16 v[94:97], v[164:167], v[180:183], v[94:97]
	v_mfma_f32_16x16x32_bf16 v[94:97], v[168:171], v[184:187], v[94:97]
	v_mfma_f32_16x16x32_bf16 v[102:105], v[160:163], v[184:187], v[102:105]
	v_mfma_f32_16x16x32_bf16 v[102:105], v[156:159], v[180:183], v[102:105]
	v_mfma_f32_16x16x32_bf16 v[106:109], v[148:151], v[180:183], v[106:109]
	v_mfma_f32_16x16x32_bf16 v[106:109], v[152:155], v[184:187], v[106:109]
	s_waitcnt lgkmcnt(0)
	v_mfma_f32_16x16x32_bf16 v[114:117], v[144:147], v[184:187], v[114:117]
	v_mfma_f32_16x16x32_bf16 v[114:117], v[140:143], v[180:183], v[114:117]
	v_mfma_f32_16x16x32_bf16 v[98:101], v[140:143], v[188:191], v[98:101]
	v_mfma_f32_16x16x32_bf16 v[98:101], v[144:147], v[192:195], v[98:101]
	v_mfma_f32_16x16x32_bf16 v[90:93], v[152:155], v[192:195], v[90:93]
	v_mfma_f32_16x16x32_bf16 v[90:93], v[148:151], v[188:191], v[90:93]
	v_mfma_f32_16x16x32_bf16 v[86:89], v[156:159], v[188:191], v[86:89]
	v_mfma_f32_16x16x32_bf16 v[86:89], v[160:163], v[192:195], v[86:89]
	v_mfma_f32_16x16x32_bf16 v[78:81], v[168:171], v[192:195], v[78:81]
	v_mfma_f32_16x16x32_bf16 v[78:81], v[164:167], v[188:191], v[78:81]
	v_mfma_f32_16x16x32_bf16 v[66:69], v[164:167], v[196:199], v[66:69]
	v_mfma_f32_16x16x32_bf16 v[66:69], v[168:171], v[200:203], v[66:69]
	v_mfma_f32_16x16x32_bf16 v[70:73], v[160:163], v[200:203], v[70:73]
	v_mfma_f32_16x16x32_bf16 v[70:73], v[156:159], v[196:199], v[70:73]
	v_mfma_f32_16x16x32_bf16 v[74:77], v[148:151], v[196:199], v[74:77]
	v_mfma_f32_16x16x32_bf16 v[74:77], v[152:155], v[200:203], v[74:77]
	v_mfma_f32_16x16x32_bf16 v[82:85], v[144:147], v[200:203], v[82:85]
	v_mfma_f32_16x16x32_bf16 v[82:85], v[140:143], v[196:199], v[82:85]
	s_barrier
	s_mov_b32 m0, s34
	s_or_b32 s53, s52, 0x80
	ds_read_b128 v[172:175], v139 offset:49152
	ds_read_b128 v[176:179], v139 offset:50176
	ds_read_b128 v[180:183], v139 offset:51200
	ds_read_b128 v[184:187], v139 offset:52224
	ds_read_b128 v[188:191], v139 offset:53248
	ds_read_b128 v[192:195], v139 offset:54272
	ds_read_b128 v[196:199], v139 offset:55296
	ds_read_b128 v[200:203], v139 offset:56320
	buffer_load_dwordx4 v135, s[8:11], s53 offen lds
	s_mov_b32 m0, s35
	s_add_i32 s52, s52, 0x200080
	buffer_load_dwordx4 v137, s[8:11], s53 offen lds
	s_mov_b32 m0, s39
	s_nop 0
	buffer_load_dwordx4 v135, s[8:11], s52 offen lds
	s_mov_b32 m0, s40
	s_nop 0
	buffer_load_dwordx4 v137, s[8:11], s52 offen lds
	s_mov_b32 m0, s37
	s_nop 0
	buffer_load_dwordx4 v134, s[4:7], s51 offen lds
	s_mov_b32 m0, s38
	s_nop 0
	buffer_load_dwordx4 v136, s[4:7], s51 offen lds
	s_waitcnt vmcnt(8)
	s_waitcnt lgkmcnt(0)
	s_barrier
	s_waitcnt lgkmcnt(7)
	v_mfma_f32_16x16x32_bf16 v[62:65], v[140:143], v[172:175], v[62:65]
	v_mfma_f32_16x16x32_bf16 v[62:65], v[144:147], v[176:179], v[62:65]
	s_waitcnt lgkmcnt(5)
	v_mfma_f32_16x16x32_bf16 v[58:61], v[152:155], v[176:179], v[58:61]
	v_mfma_f32_16x16x32_bf16 v[58:61], v[148:151], v[172:175], v[58:61]
	s_waitcnt lgkmcnt(3)
	v_mfma_f32_16x16x32_bf16 v[54:57], v[156:159], v[172:175], v[54:57]
	v_mfma_f32_16x16x32_bf16 v[54:57], v[160:163], v[176:179], v[54:57]
	s_waitcnt lgkmcnt(1)
	v_mfma_f32_16x16x32_bf16 v[46:49], v[168:171], v[176:179], v[46:49]
	v_mfma_f32_16x16x32_bf16 v[46:49], v[164:167], v[172:175], v[46:49]
	v_mfma_f32_16x16x32_bf16 v[30:33], v[164:167], v[180:183], v[30:33]
	v_mfma_f32_16x16x32_bf16 v[30:33], v[168:171], v[184:187], v[30:33]
	v_mfma_f32_16x16x32_bf16 v[38:41], v[160:163], v[184:187], v[38:41]
	v_mfma_f32_16x16x32_bf16 v[38:41], v[156:159], v[180:183], v[38:41]
	v_mfma_f32_16x16x32_bf16 v[42:45], v[148:151], v[180:183], v[42:45]
	v_mfma_f32_16x16x32_bf16 v[42:45], v[152:155], v[184:187], v[42:45]
	s_waitcnt lgkmcnt(0)
	v_mfma_f32_16x16x32_bf16 v[50:53], v[144:147], v[184:187], v[50:53]
	v_mfma_f32_16x16x32_bf16 v[50:53], v[140:143], v[180:183], v[50:53]
	v_mfma_f32_16x16x32_bf16 v[34:37], v[140:143], v[188:191], v[34:37]
	v_mfma_f32_16x16x32_bf16 v[34:37], v[144:147], v[192:195], v[34:37]
	v_mfma_f32_16x16x32_bf16 v[26:29], v[152:155], v[192:195], v[26:29]
	v_mfma_f32_16x16x32_bf16 v[26:29], v[148:151], v[188:191], v[26:29]
	v_mfma_f32_16x16x32_bf16 v[22:25], v[156:159], v[188:191], v[22:25]
	v_mfma_f32_16x16x32_bf16 v[22:25], v[160:163], v[192:195], v[22:25]
	v_mfma_f32_16x16x32_bf16 v[14:17], v[168:171], v[192:195], v[14:17]
	v_mfma_f32_16x16x32_bf16 v[14:17], v[164:167], v[188:191], v[14:17]
	v_mfma_f32_16x16x32_bf16 v[2:5], v[164:167], v[196:199], v[2:5]
	v_mfma_f32_16x16x32_bf16 v[2:5], v[168:171], v[200:203], v[2:5]
	v_mfma_f32_16x16x32_bf16 v[6:9], v[160:163], v[200:203], v[6:9]
	v_mfma_f32_16x16x32_bf16 v[6:9], v[156:159], v[196:199], v[6:9]
	v_mfma_f32_16x16x32_bf16 v[10:13], v[148:151], v[196:199], v[10:13]
	v_mfma_f32_16x16x32_bf16 v[10:13], v[152:155], v[200:203], v[10:13]
	v_mfma_f32_16x16x32_bf16 v[18:21], v[144:147], v[200:203], v[18:21]
	v_mfma_f32_16x16x32_bf16 v[18:21], v[140:143], v[196:199], v[18:21]
	s_barrier
	s_add_i32 s49, s49, 2
	s_addk_i32 s50, 0x100
	s_cmpk_gt_u32 s49, 0x7d
	s_cbranch_scc0 .LBB0_1029
	s_andn2_b64 vcc, exec, s[2:3]
	s_cbranch_vccnz .LBB0_1021
	v_mov_b32_e32 v2, 0
	s_mov_b32 s17, s44
	s_mov_b32 s14, s45
	s_mov_b32 s25, s46
	s_mov_b32 s30, s13
	s_mov_b32 s43, s12
	v_mov_b32_e32 v3, v2
	v_mov_b32_e32 v4, v2
	v_mov_b32_e32 v5, v2
	v_mov_b32_e32 v6, v2
	v_mov_b32_e32 v7, v2
	v_mov_b32_e32 v8, v2
	v_mov_b32_e32 v9, v2
	v_mov_b32_e32 v14, v2
	v_mov_b32_e32 v15, v2
	v_mov_b32_e32 v16, v2
	v_mov_b32_e32 v17, v2
	v_mov_b32_e32 v22, v2
	v_mov_b32_e32 v23, v2
	v_mov_b32_e32 v24, v2
	v_mov_b32_e32 v25, v2
	v_mov_b32_e32 v30, v2
	v_mov_b32_e32 v31, v2
	v_mov_b32_e32 v32, v2
	v_mov_b32_e32 v33, v2
	v_mov_b32_e32 v38, v2
	v_mov_b32_e32 v39, v2
	v_mov_b32_e32 v40, v2
	v_mov_b32_e32 v41, v2
	v_mov_b32_e32 v46, v2
	v_mov_b32_e32 v47, v2
	v_mov_b32_e32 v48, v2
	v_mov_b32_e32 v49, v2
	v_mov_b32_e32 v54, v2
	v_mov_b32_e32 v55, v2
	v_mov_b32_e32 v56, v2
	v_mov_b32_e32 v57, v2
	v_mov_b32_e32 v10, v2
	v_mov_b32_e32 v11, v2
	v_mov_b32_e32 v12, v2
	v_mov_b32_e32 v13, v2
	v_mov_b32_e32 v18, v2
	v_mov_b32_e32 v19, v2
	v_mov_b32_e32 v20, v2
	v_mov_b32_e32 v21, v2
	v_mov_b32_e32 v26, v2
	v_mov_b32_e32 v27, v2
	v_mov_b32_e32 v28, v2
	v_mov_b32_e32 v29, v2
	v_mov_b32_e32 v34, v2
	v_mov_b32_e32 v35, v2
	v_mov_b32_e32 v36, v2
	v_mov_b32_e32 v37, v2
	v_mov_b32_e32 v42, v2
	v_mov_b32_e32 v43, v2
	v_mov_b32_e32 v44, v2
	v_mov_b32_e32 v45, v2
	v_mov_b32_e32 v50, v2
	v_mov_b32_e32 v51, v2
	v_mov_b32_e32 v52, v2
	v_mov_b32_e32 v53, v2
	v_mov_b32_e32 v58, v2
	v_mov_b32_e32 v59, v2
	v_mov_b32_e32 v60, v2
	v_mov_b32_e32 v61, v2
	v_mov_b32_e32 v62, v2
	v_mov_b32_e32 v63, v2
	v_mov_b32_e32 v64, v2
	v_mov_b32_e32 v65, v2
	v_mov_b32_e32 v66, v2
	v_mov_b32_e32 v67, v2
	v_mov_b32_e32 v68, v2
	v_mov_b32_e32 v69, v2
	v_mov_b32_e32 v70, v2
	v_mov_b32_e32 v71, v2
	v_mov_b32_e32 v72, v2
	v_mov_b32_e32 v73, v2
	v_mov_b32_e32 v78, v2
	v_mov_b32_e32 v79, v2
	v_mov_b32_e32 v80, v2
	v_mov_b32_e32 v81, v2
	v_mov_b32_e32 v86, v2
	v_mov_b32_e32 v87, v2
	v_mov_b32_e32 v88, v2
	v_mov_b32_e32 v89, v2
	v_mov_b32_e32 v94, v2
	v_mov_b32_e32 v95, v2
	v_mov_b32_e32 v96, v2
	v_mov_b32_e32 v97, v2
	v_mov_b32_e32 v102, v2
	v_mov_b32_e32 v103, v2
	v_mov_b32_e32 v104, v2
	v_mov_b32_e32 v105, v2
	v_mov_b32_e32 v110, v2
	v_mov_b32_e32 v111, v2
	v_mov_b32_e32 v112, v2
	v_mov_b32_e32 v113, v2
	v_mov_b32_e32 v118, v2
	v_mov_b32_e32 v119, v2
	v_mov_b32_e32 v120, v2
	v_mov_b32_e32 v121, v2
	v_mov_b32_e32 v74, v2
	v_mov_b32_e32 v75, v2
	v_mov_b32_e32 v76, v2
	v_mov_b32_e32 v77, v2
	v_mov_b32_e32 v82, v2
	v_mov_b32_e32 v83, v2
	v_mov_b32_e32 v84, v2
	v_mov_b32_e32 v85, v2
	v_mov_b32_e32 v90, v2
	v_mov_b32_e32 v91, v2
	v_mov_b32_e32 v92, v2
	v_mov_b32_e32 v93, v2
	v_mov_b32_e32 v98, v2
	v_mov_b32_e32 v99, v2
	v_mov_b32_e32 v100, v2
	v_mov_b32_e32 v101, v2
	v_mov_b32_e32 v106, v2
	v_mov_b32_e32 v107, v2
	v_mov_b32_e32 v108, v2
	v_mov_b32_e32 v109, v2
	v_mov_b32_e32 v114, v2
	v_mov_b32_e32 v115, v2
	v_mov_b32_e32 v116, v2
	v_mov_b32_e32 v117, v2
	v_mov_b32_e32 v122, v2
	v_mov_b32_e32 v123, v2
	v_mov_b32_e32 v124, v2
	v_mov_b32_e32 v125, v2
	v_mov_b32_e32 v126, v2
	v_mov_b32_e32 v127, v2
	v_mov_b32_e32 v128, v2
	v_mov_b32_e32 v129, v2
	s_branch .LBB0_1021
